# baseline (speedup 1.0000x reference)
.LBB1_107:
	v_and_b32_e32 v98, 48, v179
	v_readlane_b32 s18, v240, 24
	v_add_u32_e32 v108, 0, v98
	v_add_u32_e32 v108, 0x18400, v108
	v_add_u32_e32 v162, s18, v98
	s_waitcnt lgkmcnt(0)
	s_barrier
	ds_read_b128 v[138:141], v108
	ds_read_b128 v[142:145], v108 offset:64
	ds_read_b128 v[146:149], v108 offset:128
	ds_read_b128 v[150:153], v108 offset:192
	ds_read_b128 v[154:157], v162
	ds_read_b128 v[158:161], v162 offset:64
	s_waitcnt vmcnt(7) lgkmcnt(5)
	v_mfma_f32_16x16x32_f16 v[130:133], v[130:133], v[138:141], 0
	s_waitcnt vmcnt(3)
	v_mfma_f32_16x16x32_f16 v[134:137], v[134:137], v[138:141], 0
	s_waitcnt lgkmcnt(4)
	v_mfma_f32_16x16x32_f16 v[114:117], v[114:117], v[142:145], v[130:133]
	s_waitcnt vmcnt(2)
	v_mfma_f32_16x16x32_f16 v[122:125], v[122:125], v[142:145], v[134:137]
	s_waitcnt lgkmcnt(3)
	v_mfma_f32_16x16x32_f16 v[114:117], v[118:121], v[146:149], v[114:117]
	s_waitcnt vmcnt(1)
	v_mfma_f32_16x16x32_f16 v[118:121], v[126:129], v[146:149], v[122:125]
	s_waitcnt lgkmcnt(2)
	v_mfma_f32_16x16x32_f16 v[114:117], v[104:107], v[150:153], v[114:117]
	v_and_b32_e32 v104, 15, v179
	v_cmp_gt_u32_e32 vcc, 2, v104
	s_waitcnt vmcnt(0)
	v_mfma_f32_16x16x32_f16 v[104:107], v[110:113], v[150:153], v[118:121]
	s_and_saveexec_b64 s[0:1], vcc
	s_cbranch_execz .LBB1_115
	s_cmp_lg_u32 s30, 31
	v_lshrrev_b32_e32 v103, 2, v103
	s_nop 7
	s_cselect_b64 s[20:21], -1, 0
	s_and_b64 vcc, exec, s[20:21]
	s_waitcnt lgkmcnt(0)
	v_and_b32_e32 v162, 1, v179
	v_cmp_eq_u32_e64 s[100:101], 1, v162
	s_nop 1
	v_cndmask_b32_e64 v163, 0, 16, s[100:101]
	v_cndmask_b32_e64 v114, v114, v104, s[100:101]
	v_cndmask_b32_e64 v154, v154, v158, s[100:101]
	v_cndmask_b32_e64 v115, v115, v105, s[100:101]
	v_cndmask_b32_e64 v155, v155, v159, s[100:101]
	v_cndmask_b32_e64 v116, v116, v106, s[100:101]
	v_cndmask_b32_e64 v156, v156, v160, s[100:101]
	v_cndmask_b32_e64 v117, v117, v107, s[100:101]
	v_cndmask_b32_e64 v157, v157, v161, s[100:101]
	v_add_f32_e32 v108, v114, v154
	v_add_f32_e32 v110, v115, v155
	v_add_f32_e32 v108, v108, v108
	v_add_f32_e32 v110, v110, v110
	v_mul_f32_e32 v108, 0x3fb8aa3b, v108
	v_exp_f32_e32 v108, v108
	v_mul_f32_e32 v110, 0x3fb8aa3b, v110
	v_exp_f32_e32 v115, v110
	v_add_f32_e32 v98, 1.0, v108
	v_add_f32_e32 v108, v116, v156
	v_rcp_f32_e32 v114, v98
	v_add_f32_e32 v98, 1.0, v115
	v_add_f32_e32 v108, v108, v108
	v_add_f32_e32 v115, v117, v157
	v_mul_f32_e32 v108, 0x3fb8aa3b, v108
	v_add_f32_e32 v115, v115, v115
	v_exp_f32_e32 v108, v108
	v_mul_f32_e32 v115, 0x3fb8aa3b, v115
	v_exp_f32_e32 v117, v115
	v_rcp_f32_e32 v115, v98
	v_add_f32_e32 v98, 1.0, v108
	v_rcp_f32_e32 v116, v98
	v_add_f32_e32 v98, 1.0, v117
	v_rcp_f32_e32 v117, v98
	v_or_b32_e32 v98, s71, v103
	v_add_u32_e32 v98, v98, v163
	v_pk_fma_f32 v[114:115], v[114:115], 2.0, 1.0 op_sel_hi:[1,0,0] neg_lo:[1,0,0] neg_hi:[1,0,0]
	v_pk_fma_f32 v[116:117], v[116:117], 2.0, 1.0 op_sel_hi:[1,0,0] neg_lo:[1,0,0] neg_hi:[1,0,0]
	s_cbranch_vccnz .LBB1_110
	v_readlane_b32 s18, v240, 18
	v_mov_b32_e32 v119, v99
	v_readlane_b32 s19, v240, 19
	v_add_u32_e32 v118, s18, v98
	v_lshl_add_u64 v[118:119], v[118:119], 2, s[60:61]
	global_store_dwordx4 v[118:119], v[114:117], off
.LBB1_110:
	v_cvt_pk_f16_f32 v118, v114, v115
	v_cvt_f32_f16_e32 v120, v118
	v_cvt_f32_f16_sdwa v121, v118 dst_sel:DWORD dst_unused:UNUSED_PAD src0_sel:WORD_1
	v_cvt_pk_f16_f32 v119, v116, v117
	v_readlane_b32 s18, v240, 25
	s_add_u32 s96, s18, s98
	v_pk_add_f32 v[114:115], v[114:115], v[120:121] neg_lo:[0,1] neg_hi:[0,1]
	v_cvt_f32_f16_e32 v120, v119
	v_cvt_f32_f16_sdwa v121, v119 dst_sel:DWORD dst_unused:UNUSED_PAD src0_sel:WORD_1
	v_readlane_b32 s18, v240, 26
	v_lshrrev_b32_e32 v122, 1, v179
	s_addc_u32 s97, s18, s99
	v_pk_add_f32 v[116:117], v[116:117], v[120:121] neg_lo:[0,1] neg_hi:[0,1]
	v_pk_mul_f32 v[114:115], v[114:115], s[94:95] op_sel_hi:[1,0]
	v_pk_mul_f32 v[116:117], v[116:117], s[94:95] op_sel_hi:[1,0]
	v_and_b32_e32 v108, 4, v103
	v_cvt_pk_f16_f32 v114, v114, v115
	v_cvt_pk_f16_f32 v115, v116, v117
	v_lshl_add_u64 v[116:117], v[98:99], 1, s[96:97]
	v_and_or_b32 v98, v122, 16, s33
	s_add_u32 s18, s48, s9
	global_store_dwordx2 v[116:117], v[118:119], off
	v_lshl_or_b32 v116, v98, 3, v108
	v_lshl_add_u32 v116, v163, 4, v116
	s_addc_u32 s19, s49, 0
	v_ashrrev_i32_e32 v117, 31, v116
	v_lshl_add_u64 v[116:117], v[116:117], 1, s[18:19]
	global_store_dwordx2 v[116:117], v[118:119], off sc0 sc1
	s_mov_b64 s[98:99], 0x20000
	v_lshl_add_u64 v[116:117], v[116:117], 0, s[98:99]
	global_store_dwordx2 v[116:117], v[114:115], off sc0 sc1
